# routing-table phase: the 16 count loads of a totals-loop iteration issued together (1 round trip instead of 4); state GEMM scheduler skips the 128 units whose outputs nothing reads (exactly 4 rounds)
# baseline (speedup 1.0000x reference)
.LBB0_1239:
	v_mbcnt_lo_u32_b32 v0, -1, 0
	v_mbcnt_hi_u32_b32 v0, -1, v0
	s_cmpk_gt_i32 s94, 0x3ff
	v_add_u32_e32 v1, s52, v0
	s_nop 0
	v_readfirstlane_b32 s6, v1
	s_cbranch_scc1 .LBB0_1260
	s_lshr_b32 s11, s94, 4
	s_and_b32 s9, s94, 15
	s_cmp_gt_u32 s9, 2
	s_addc_u32 s9, s9, 0
	s_cmp_gt_u32 s9, 15
	s_addc_u32 s9, s9, 0
	v_ashrrev_i32_e32 v3, 31, v1
	s_ashr_i32 s10, s6, 6
	v_lshrrev_b32_e32 v3, 26, v3
	s_ashr_i32 s7, s6, 8
	v_lshlrev_b32_e32 v2, 4, v1
	v_add_u32_e32 v3, v1, v3
	v_bfe_i32 v1, v1, 27, 1
	s_lshl_b32 s33, s10, 10
	s_ashr_i32 s12, s9, 1
	s_and_b32 s13, s9, 1
	s_ashr_i32 s8, s11, 2
	v_lshrrev_b32_e32 v1, 22, v1
	s_cmp_lt_u32 s9, 2
	v_add_u32_e32 v1, v2, v1
	s_cselect_b64 s[14:15], -1, 0
	s_lshl_b32 s9, s11, 3
	s_add_i32 s18, s12, -1
	v_and_b32_e32 v1, 0xfffffc00, v1
	s_add_i32 s9, s18, s9
	v_sub_u32_e32 v1, v2, v1
	s_and_b64 s[16:17], s[14:15], exec
	s_mov_b32 s46, 0x62000000
	s_waitcnt vmcnt(0)
	v_lshrrev_b32_e32 v4, 4, v1
	s_cselect_b32 s16, s46, 0x56000000
	v_bitop3_b32 v1, v4, v1, 32 bitop3:0x6c
	s_cselect_b32 s9, s11, s9
	s_add_u32 s16, s26, s16
	v_ashrrev_i32_e32 v5, 31, v1
	s_addc_u32 s17, s27, 0
	s_mul_hi_i32 s19, s9, 0x60000
	s_mul_i32 s9, s9, 0x60000
	v_ashrrev_i32_e32 v3, 6, v3
	v_lshrrev_b32_e32 v5, 26, v5
	s_add_u32 s38, s16, s9
	v_lshlrev_b32_e32 v4, 3, v3
	v_add_u32_e32 v5, v1, v5
	s_addc_u32 s39, s17, s19
	s_ashr_i32 s9, s8, 31
	v_and_b32_e32 v4, -16, v4
	v_ashrrev_i32_e32 v6, 6, v5
	v_add_u32_e32 v2, 0x2000, v2
	s_lshl_b64 s[16:17], s[8:9], 11
	v_add_u32_e32 v7, v6, v4
	v_and_b32_e32 v4, 0xc0, v5
	v_ashrrev_i32_e32 v5, 31, v2
	s_and_b64 s[14:15], s[14:15], exec
	v_lshrrev_b32_e32 v5, 22, v5
	s_cselect_b32 s8, s8, s18
	v_add_u32_e32 v5, v2, v5
	s_cselect_b32 s15, 0, s17
	s_cselect_b32 s14, 0x8000, s16
	s_ashr_i32 s9, s8, 31
	v_ashrrev_i32_e32 v5, 10, v5
	s_cmp_eq_u32 s13, 0
	s_mov_b32 s47, 0x67800000
	v_mul_i32_i24_e32 v8, 0x400, v5
	s_cselect_b32 s16, s47, 0x6c000000
	v_sub_u32_e32 v2, v2, v8
	s_add_u32 s16, s26, s16
	v_lshrrev_b32_e32 v8, 4, v2
	s_addc_u32 s17, s27, 0
	s_lshl_b32 s18, s11, 8
	v_bitop3_b32 v2, v8, v2, 32 bitop3:0x6c
	s_and_b32 s18, s18, 0x300
	v_ashrrev_i32_e32 v9, 31, v2
	s_mul_i32 s18, s18, 0x9000
	v_lshrrev_b32_e32 v9, 26, v9
	s_add_u32 s14, s14, s18
	v_add_u32_e32 v9, v2, v9
	s_addc_u32 s15, s15, 0
	v_ashrrev_i32_e32 v10, 6, v9
	v_and_b32_e32 v9, 0xc0, v9
	s_lshl_b64 s[8:9], s[8:9], 9
	s_lshl_b64 s[14:15], s[14:15], 1
	v_sub_u32_e32 v1, v1, v4
	v_mov_b32_e32 v4, 1
	v_sub_u32_e32 v2, v2, v9
	s_add_u32 s8, s16, s8
	v_lshlrev_b32_e32 v8, 3, v5
	v_ashrrev_i16_sdwa v2, v4, sext(v2) dst_sel:DWORD dst_unused:UNUSED_PAD src0_sel:DWORD src1_sel:BYTE_0
	s_addc_u32 s9, s17, s9
	v_ashrrev_i16_sdwa v1, v4, sext(v1) dst_sel:DWORD dst_unused:UNUSED_PAD src0_sel:DWORD src1_sel:BYTE_0
	v_and_b32_e32 v8, -16, v8
	v_bfe_i32 v4, v2, 0, 16
	v_lshlrev_b32_e32 v2, 1, v7
	v_lshrrev_b32_e32 v9, 2, v7
	v_and_b32_e32 v6, 3, v6
	s_mov_b32 s3, 0x7ffe0
	s_add_u32 s44, s8, s14
	v_add_u32_e32 v8, v10, v8
	v_and_b32_e32 v2, 24, v2
	v_and_b32_e32 v9, 4, v9
	v_and_or_b32 v6, v7, s3, v6
	s_addc_u32 s45, s9, s15
	v_lshlrev_b32_e32 v3, 5, v3
	v_lshlrev_b32_e32 v5, 5, v5
	v_or3_b32 v6, v6, v9, v2
	v_lshlrev_b32_e32 v2, 1, v8
	v_lshrrev_b32_e32 v9, 2, v8
	v_and_b32_e32 v10, 3, v10
	s_add_u32 s42, s44, 0x900000
	v_and_b32_e32 v3, 32, v3
	v_bfe_i32 v1, v1, 0, 16
	v_and_b32_e32 v5, 32, v5
	v_and_b32_e32 v2, 24, v2
	v_and_b32_e32 v9, 4, v9
	v_and_or_b32 v10, v8, s3, v10
	s_addc_u32 s43, s45, 0
	v_or3_b32 v9, v10, v9, v2
	v_add_lshl_u32 v2, v3, v1, 1
	s_mov_b32 s3, 0x12000
	v_add_lshl_u32 v4, v5, v4, 1
	s_add_u32 s40, s38, 0x30000
	s_movk_i32 s14, 0x600
	v_mad_u32_u24 v134, v6, s3, v2
	v_mad_u32_u24 v135, v9, s3, v4
	s_addc_u32 s41, s39, 0
	v_mad_u64_u32 v[128:129], s[8:9], v7, s14, v[2:3]
	v_mad_u64_u32 v[130:131], s[8:9], v8, s14, v[4:5]
	s_add_i32 s48, s33, 0
	s_mov_b64 s[8:9], s[44:45]
	v_mov_b32_e32 v1, v135
	v_mov_b32_e32 v2, v134
	s_add_i32 m0, s48, 0x10000
	s_add_i32 s49, s48, 0x2000
	global_load_lds_dwordx4 v2, s[8:9]
	s_add_i32 m0, s48, 0x12000
	v_mov_b32_e32 v2, v135
	global_load_lds_dwordx4 v1, s[8:9]
	v_mov_b32_e32 v1, v134
	s_mov_b64 s[8:9], s[42:43]
	s_add_i32 m0, s48, 0x14000
	s_add_i32 s50, s48, 0x4000
	global_load_lds_dwordx4 v1, s[8:9]
	s_add_i32 m0, s48, 0x16000
	v_mov_b32_e32 v1, v130
	global_load_lds_dwordx4 v2, s[8:9]
	s_mov_b64 s[8:9], s[38:39]
	v_mov_b32_e32 v2, v128
	s_mov_b32 m0, s48
	s_add_i32 s51, s48, 0x6000
	global_load_lds_dwordx4 v2, s[8:9] nt
	s_mov_b32 m0, s49
	v_mov_b32_e32 v2, v130
	global_load_lds_dwordx4 v1, s[8:9] nt
	v_mov_b32_e32 v1, v128
	s_mov_b64 s[8:9], s[40:41]
	s_mov_b32 m0, s50
	s_cmp_eq_u32 s7, 1
	global_load_lds_dwordx4 v1, s[8:9] nt
	s_mov_b32 m0, s51
	s_movk_i32 s52, 0x2000
	global_load_lds_dwordx4 v2, s[8:9] nt
	s_mov_b32 s54, 0
	s_mov_b32 s53, 0x10000
	s_mov_b32 s55, 0x14000
	s_movk_i32 s56, 0x4000
	s_cselect_b64 s[8:9], -1, 0
	s_cmp_lg_u32 s7, 1
	s_movk_i32 s57, 0x6000
	s_cbranch_scc1 .LBB0_1242
	s_barrier
.LBB0_1242:
	s_lshl_b32 s10, s10, 5
	s_and_b32 s17, s10, 0x60
	s_lshl_b32 s16, s7, 13
	s_lshl_b32 s18, s17, 7
	s_add_u32 s58, s26, 0x75000000
	s_addc_u32 s59, s27, 0
	s_lshl_b32 s10, s11, 1
	s_or_b32 s10, s10, s13
	s_mul_i32 s10, s10, 9
	s_add_i32 s10, s10, s12
	s_ashr_i32 s11, s10, 31
	s_lshl_b64 s[10:11], s[10:11], 17
	s_add_u32 s22, s58, s10
	s_addc_u32 s23, s59, s11
	s_add_u32 s10, s44, 0x80
	s_addc_u32 s11, s45, 0
	s_add_u32 s12, s38, 0x80
	s_addc_u32 s13, s39, 0
	s_add_u32 s14, s44, 0x900080
	s_addc_u32 s15, s45, 0
	v_mov_b32_e32 v1, v134
	v_mov_b32_e32 v2, v135
	s_add_i32 m0, s48, 0x18000
	s_waitcnt vmcnt(2)
	s_barrier
	s_add_i32 s60, s48, 0x8000
	global_load_lds_dwordx4 v1, s[10:11]
	s_add_i32 m0, s48, 0x1a000
	v_mov_b32_e32 v1, v130
	global_load_lds_dwordx4 v2, s[10:11]
	v_mov_b32_e32 v2, v128
	s_mov_b32 m0, s60
	s_add_i32 s61, s48, 0xa000
	v_mov_b64_e32 v[132:133], 0x3ff
	global_load_lds_dwordx4 v2, s[12:13] nt
	s_mov_b32 m0, s61
	v_mov_b32_e32 v2, v134
	global_load_lds_dwordx4 v1, s[12:13] nt
	v_mov_b32_e32 v1, v135
	s_add_i32 m0, s48, 0x1c000
	s_nop 0
	global_load_lds_dwordx4 v2, s[14:15]
	s_add_i32 m0, s48, 0x1e000
	v_lshrrev_b32_e32 v2, 1, v0
	global_load_lds_dwordx4 v1, s[14:15]
	v_and_b32_e32 v2, 24, v2
	s_cmp_gt_i32 s2, 0
	v_and_b32_e32 v1, 15, v0
	v_lshlrev_b32_e32 v3, 1, v2
	v_lshlrev_b32_e32 v0, 2, v0
	s_cselect_b64 s[10:11], -1, 0
	s_add_i32 s62, s2, -2
	v_lshl_or_b32 v129, s7, 6, v1
	v_lshl_or_b32 v1, v1, 6, v3
	v_and_b32_e32 v0, 32, v0
	s_waitcnt vmcnt(6)
	s_cmpk_lt_u32 s6, 0x100
	v_bitop3_b32 v3, v1, s16, v0 bitop3:0xde
	v_bitop3_b32 v131, v1, s18, v0 bitop3:0xde
	s_cselect_b64 s[12:13], -1, 0
	s_add_i32 s63, 0, 0x10000
	s_add_i32 s64, 0, 0x14000
	v_or_b32_e32 v136, s17, v2
	v_add_u32_e32 v137, s63, v131
	v_add_u32_e32 v138, s64, v131
	v_add_u32_e32 v139, 0, v3
	s_barrier
	s_branch .LBB0_1245

.LBB0_1245:
	s_mov_b32 s6, s54
	s_add_i32 s54, s54, 1
	s_cmp_gt_u32 s6, 0x3ffffffe
	s_mov_b64 s[28:29], 0
	s_cbranch_scc1 .LBB0_1248
	s_load_dword s28, s[90:91], 0x100
	s_mul_i32 s6, s54, s0
	s_waitcnt lgkmcnt(0)
	s_mul_hi_u32 s7, s54, s28
	s_add_i32 s7, s7, s6
	s_mul_i32 s6, s54, s28
	s_add_u32 s6, s6, s94
	s_addc_u32 s7, s7, s1
	v_cmp_gt_i64_e32 vcc, s[6:7], v[132:133]
	s_mov_b64 s[28:29], 0
	s_cbranch_vccnz .LBB0_1248
	s_lshr_b32 s20, s6, 4
	s_and_b32 s7, s6, 15
	s_cmp_gt_u32 s7, 2
	s_addc_u32 s7, s7, 0
	s_cmp_gt_u32 s7, 15
	s_addc_u32 s7, s7, 0
	s_ashr_i32 s21, s7, 1
	s_and_b32 s28, s7, 1
	s_ashr_i32 s6, s20, 2
	s_cmp_lt_u32 s7, 2
	s_cselect_b64 s[16:17], -1, 0
	s_lshl_b32 s7, s20, 3
	s_add_i32 s29, s21, -1
	s_add_i32 s7, s29, s7
	s_and_b64 s[14:15], s[16:17], exec
	s_cselect_b32 s14, s46, 0x56000000
	s_cselect_b32 s7, s20, s7
	s_add_u32 s14, s26, s14
	s_addc_u32 s15, s27, 0
	s_mul_hi_i32 s18, s7, 0x60000
	s_mul_i32 s7, s7, 0x60000
	s_add_u32 s14, s14, s7
	s_addc_u32 s15, s15, s18
	s_ashr_i32 s7, s6, 31
	s_lshl_b64 s[18:19], s[6:7], 11
	s_and_b64 s[16:17], s[16:17], exec
	s_cselect_b32 s6, s6, s29
	s_cselect_b32 s17, 0, s19
	s_cselect_b32 s16, 0x8000, s18
	s_ashr_i32 s7, s6, 31
	s_cmp_eq_u32 s28, 0
	s_cselect_b32 s18, s47, 0x6c000000
	s_add_u32 s18, s26, s18
	s_addc_u32 s19, s27, 0
	s_lshl_b32 s29, s20, 8
	s_and_b32 s29, s29, 0x300
	s_mul_i32 s29, s29, 0x9000
	s_add_u32 s16, s16, s29
	s_addc_u32 s17, s17, 0
	s_lshl_b64 s[6:7], s[6:7], 9
	s_lshl_b64 s[16:17], s[16:17], 1
	s_add_u32 s6, s18, s6
	s_addc_u32 s7, s19, s7
	s_add_u32 s16, s6, s16
	s_addc_u32 s17, s7, s17
	s_add_u32 s18, s16, 0x900000
	s_addc_u32 s19, s17, 0
	s_lshl_b32 s6, s20, 1
	s_or_b32 s6, s6, s28
	s_mul_i32 s6, s6, 9
	s_add_i32 s6, s6, s21
	s_ashr_i32 s7, s6, 31
	s_lshl_b64 s[6:7], s[6:7], 17
	s_add_u32 s20, s58, s6
	s_addc_u32 s21, s59, s7
	s_mov_b64 s[28:29], -1

.LBB0_2008:
	v_lshlrev_b32_e32 v4, 3, v1
	v_lshlrev_b32_e32 v2, 3, v0
	v_ashrrev_i32_e32 v3, 31, v2
	v_ashrrev_i32_e32 v5, 31, v4
	v_lshlrev_b64 v[24:25], 7, v[4:5]
	v_lshlrev_b64 v[26:27], 7, v[2:3]
	v_lshl_add_u64 v[26:27], v[14:15], 0, v[26:27]
	v_lshl_add_u64 v[24:25], v[14:15], 0, v[24:25]
	global_load_dword v89, v[26:27], off
	global_load_dword v90, v[26:27], off offset:128
	global_load_dword v91, v[26:27], off offset:256
	global_load_dword v92, v[26:27], off offset:384
	global_load_dword v93, v[26:27], off offset:512
	global_load_dword v94, v[26:27], off offset:640
	global_load_dword v95, v[26:27], off offset:768
	global_load_dword v96, v[26:27], off offset:896
	global_load_dword v97, v[24:25], off
	global_load_dword v98, v[24:25], off offset:128
	global_load_dword v99, v[24:25], off offset:256
	global_load_dword v100, v[24:25], off offset:384
	global_load_dword v101, v[24:25], off offset:512
	global_load_dword v102, v[24:25], off offset:640
	global_load_dword v103, v[24:25], off offset:768
	global_load_dword v104, v[24:25], off offset:896
	v_cmp_gt_i32_e64 s[20:21], s33, v1
	v_cmp_gt_i32_e32 vcc, s1, v0
	v_add_u32_e32 v7, -2, v7
	v_add_u32_e32 v1, 2, v1
	v_add_u32_e32 v0, 2, v0
	s_waitcnt vmcnt(8)
	v_add_u32_e32 v2, v89, v90
	v_add3_u32 v2, v2, v91, v92
	v_add3_u32 v2, v2, v93, v94
	v_add3_u32 v2, v2, v95, v96
	s_waitcnt vmcnt(0)
	v_add_u32_e32 v3, v97, v98
	v_add3_u32 v3, v3, v99, v100
	v_add3_u32 v3, v3, v101, v102
	v_add3_u32 v3, v3, v103, v104
	v_add_u32_e32 v9, v3, v9
	v_add_u32_e32 v6, v2, v6
	v_cndmask_b32_e32 v2, 0, v2, vcc
	v_cndmask_b32_e64 v3, 0, v3, s[20:21]
	v_cmp_eq_u32_e32 vcc, 0, v7
	v_add_u32_e32 v22, v3, v22
	v_add_u32_e32 v12, v2, v12
	s_or_b64 s[46:47], vcc, s[46:47]
	s_andn2_b64 exec, exec, s[46:47]
	s_cbranch_execnz .LBB0_2008
	s_or_b64 exec, exec, s[46:47]
	v_readlane_b32 s20, v254, 33
	v_readlane_b32 s21, v254, 34
	v_add_u32_e32 v3, v6, v9
	v_add_u32_e32 v2, v12, v22
	s_orn2_b64 s[46:47], s[20:21], exec
	v_mov_b32_e32 v4, v53
